# K-read pipelining + static s_setprio 1 for waves 4-7 in the differential-attention tile loop
# speedup vs baseline: 1.0061x; 1.0061x over previous
.LBB0_181:
	s_or_b64 exec, exec, s[30:31]
	v_cmp_eq_u32_e32 vcc, 0, v2
	s_and_saveexec_b64 s[4:5], vcc
	v_mov_b32_e32 v0, s77
	ds_write_b32 v0, v1
	s_or_b64 exec, exec, s[4:5]
	s_ashr_i32 s4, s3, 2
	s_ashr_i32 s89, s6, 6
	s_ashr_i32 s5, s4, 31
	s_lshl_b32 s95, s74, 8
	s_lshl_b32 s72, s89, 5
	s_lshl_b64 s[30:31], s[4:5], 12
	s_add_i32 s72, s72, s95
	s_mul_i32 s91, s4, 0x1800000
	s_mul_hi_i32 s88, s4, 0x1800000
	s_add_u32 s3, s10, s91
	s_addc_u32 s5, s11, s88
	s_lshl_b32 s94, s75, 8
	s_add_u32 s4, s3, s94
	s_addc_u32 s5, s5, 0
	s_lshl_b32 s3, s89, 3
	v_bfe_u32 v236, v2, 4, 2
	v_or_b32_e32 v0, s3, v236
	v_and_b32_e32 v5, 15, v2
	v_bitop3_b32 v5, v0, v5, 11 bitop3:0x6c
	v_lshlrev_b32_e32 v237, 3, v5
	v_bfe_u32 v5, v2, 2, 3
	v_bitop3_b32 v5, s3, -13, v5 bitop3:0xc8
	s_lshl_b32 s3, s89, 2
	s_and_b32 s42, s3, 4
	s_ashr_i32 s3, s72, 31
	s_add_u32 s38, s30, s72
	s_addc_u32 s39, s31, s3
	s_mul_i32 s3, s39, 0x1800
	s_mul_hi_u32 s7, s38, 0x1800
	s_add_i32 s7, s7, s3
	s_mul_i32 s3, s38, 0x1800
	s_add_u32 s3, s10, s3
	v_and_b32_e32 v3, 31, v2
	v_lshrrev_b32_e32 v20, 1, v2
	v_lshlrev_b32_e32 v7, 3, v2
	s_addc_u32 s7, s11, s7
	v_mul_lo_u32 v0, v0, s78
	v_and_b32_e32 v238, 24, v7
	s_add_u32 s34, s3, s94
	v_mul_u32_u24_e32 v7, 0xc00, v3
	v_and_b32_e32 v22, 16, v20
	v_or_b32_e32 v0, v237, v0
	s_addc_u32 s35, s7, 0
	v_lshl_or_b32 v7, v7, 1, v22
	s_lshl_b32 s40, s89, 11
	v_lshlrev_b64 v[10:11], 1, v[0:1]
	global_load_dwordx4 v[176:179], v7, s[34:35]
	global_load_dwordx4 v[180:183], v7, s[34:35] offset:32
	global_load_dwordx4 v[184:187], v7, s[34:35] offset:64
	global_load_dwordx4 v[188:191], v7, s[34:35] offset:96
	global_load_dwordx4 v[192:195], v7, s[34:35] offset:128
	global_load_dwordx4 v[196:199], v7, s[34:35] offset:160
	global_load_dwordx4 v[200:203], v7, s[34:35] offset:192
	global_load_dwordx4 v[204:207], v7, s[34:35] offset:224
	v_lshl_add_u64 v[12:13], s[4:5], 0, v[10:11]
	s_add_i32 s7, s40, 0
	v_mov_b32_e32 v7, 0x3000
	v_and_b32_e32 v21, 8, v20
	v_lshl_add_u64 v[12:13], v[12:13], 0, s[16:17]
	s_mov_b32 m0, s7
	v_xad_u32 v0, v0, 32, v7
	v_or3_b32 v6, v21, v5, s42
	global_load_lds_dwordx4 v[12:13], off
	v_lshlrev_b64 v[12:13], 1, v[0:1]
	v_mul_lo_u32 v6, v6, s78
	v_and_b32_e32 v239, 32, v2
	v_lshl_add_u64 v[14:15], s[4:5], 0, v[12:13]
	v_or3_b32 v6, v239, v238, v6
	v_lshl_add_u64 v[14:15], v[14:15], 0, s[16:17]
	s_add_i32 m0, s7, 0x400
	v_mov_b32_e32 v7, v1
	global_load_lds_dwordx4 v[14:15], off
	v_lshlrev_b64 v[14:15], 1, v[6:7]
	v_lshl_add_u64 v[16:17], s[4:5], 0, v[14:15]
	s_add_i32 s3, s79, s40
	s_or_b32 s41, s40, 0x400
	v_lshl_add_u64 v[18:19], v[16:17], 0, s[18:19]
	s_mov_b32 m0, s3
	v_lshl_add_u64 v[16:17], v[16:17], 0, s[20:21]
	global_load_lds_dwordx4 v[18:19], off
	s_add_i32 m0, s79, s41
	s_add_u32 s36, s4, 0x60400
	s_addc_u32 s37, s5, 0
	s_add_u32 s34, s4, 0x60800
	global_load_lds_dwordx4 v[16:17], off
	s_addc_u32 s35, s5, 0
	v_lshl_add_u64 v[10:11], s[36:37], 0, v[10:11]
	s_add_i32 m0, s7, 0x4000
	v_or_b32_e32 v6, 64, v6
	global_load_lds_dwordx4 v[10:11], off
	v_lshl_add_u64 v[10:11], s[36:37], 0, v[12:13]
	s_add_i32 m0, s7, 0x4400
	v_lshl_add_u64 v[6:7], v[6:7], 1, s[34:35]
	global_load_lds_dwordx4 v[10:11], off
	v_lshl_add_u64 v[10:11], s[34:35], 0, v[14:15]
	s_add_i32 m0, s80, s40
	v_lshl_add_u32 v225, v3, 8, 0
	global_load_lds_dwordx4 v[10:11], off
	s_add_i32 m0, s80, s41
	v_lshlrev_b32_e32 v3, 2, v3
	global_load_lds_dwordx4 v[6:7], off
	v_and_b32_e32 v6, 63, v2
	v_cndmask_b32_e64 v7, v8, v9, s[0:1]
	v_sub_f32_e32 v223, v7, v4
	v_lshlrev_b32_e32 v4, 3, v6
	v_lshlrev_b32_e32 v6, 4, v2
	v_and_b32_e32 v7, 0xc0, v6
	v_lshlrev_b32_e32 v2, 1, v2
	v_and_or_b32 v7, v4, 24, v7
	v_and_b32_e32 v2, 32, v2
	v_and_b32_e32 v4, 0x100, v4
	v_or3_b32 v242, v7, v2, v4
	v_and_b32_e32 v2, 0xf0, v6
	v_bitop3_b32 v226, v22, v2, s82 bitop3:0x36
	v_bitop3_b32 v227, v20, v2, 16 bitop3:0x6c
	v_bitop3_b32 v228, v22, v2, 32 bitop3:0x36
	v_bitop3_b32 v229, v22, v2, 64 bitop3:0x36
	v_bitop3_b32 v230, v22, v2, s83 bitop3:0x36
	v_bitop3_b32 v231, v22, v2, s84 bitop3:0x36
	v_bitop3_b32 v232, v22, v2, s81 bitop3:0x36
	v_bitop3_b32 v233, v22, v2, s85 bitop3:0x36
	v_add3_u32 v2, v5, v21, s42
	v_mov_b64_e32 v[4:5], 0x120c0400
	v_add_u32_e32 v224, s79, v242
	s_cmp_lt_i32 s89, 4
	s_mov_b64 s[40:41], -1
	s_mul_i32 s56, s89, 0x6000
	v_mul_lo_u32 v241, v2, s78
	v_lshl_add_u64 v[214:215], v[0:1], 1, v[4:5]
	v_sub_u32_e32 v240, v22, v3
	s_cbranch_scc1 .LBB0_203
	v_or_b32_e32 v0, v241, v239
	v_add_u32_e32 v0, v0, v238
	s_add_u32 s40, s91, s94
	v_lshlrev_b64 v[216:217], 1, v[0:1]
	s_addc_u32 s41, s88, 0
	v_mov_b32_e32 v0, s56
	s_add_u32 s40, s66, s40
	v_mad_u32_u24 v0, v236, s78, v0
	s_addc_u32 s41, s67, s41
	v_or_b32_e32 v0, v0, v237
	v_mov_b64_e32 v[2:3], 0x120c0400
	s_lshl_b32 s42, s89, 7
	v_lshl_add_u64 v[218:219], v[0:1], 1, v[2:3]
	v_subrev_u32_e32 v0, s42, v240
	s_lshl_b32 s42, s74, 10
	v_subrev_u32_e32 v0, s42, v0
	v_mov_b32_e32 v14, v1
	v_mov_b32_e32 v15, v1
	v_add_u32_e32 v243, 0, v0
	v_mov_b32_e32 v0, v1
	v_mov_b32_e32 v2, v1
	v_mov_b32_e32 v3, v1
	v_mov_b32_e32 v4, v1
	v_mov_b32_e32 v5, v1
	v_mov_b32_e32 v6, v1
	v_mov_b32_e32 v7, v1
	v_mov_b32_e32 v8, v1
	v_mov_b32_e32 v9, v1
	v_mov_b32_e32 v10, v1
	v_mov_b32_e32 v11, v1
	v_mov_b32_e32 v12, v1
	v_mov_b32_e32 v13, v1
	v_mov_b64_e32 v[126:127], v[14:15]
	v_mov_b64_e32 v[110:111], v[14:15]
	v_mov_b64_e32 v[78:79], v[14:15]
	v_mov_b64_e32 v[62:63], v[14:15]
	v_mov_b64_e32 v[30:31], v[14:15]
	v_mov_b64_e32 v[46:47], v[14:15]
	v_mov_b64_e32 v[94:95], v[14:15]
	v_mov_b64_e32 v[142:143], v[14:15]
	s_mov_b32 s71, 0
	s_sub_i32 s73, 0, s72
	s_mov_b32 s90, 0x8000
	s_mov_b32 s44, 0xc000
	v_mov_b32_e32 v234, 0
	v_mov_b32_e32 v235, 0
	v_mov_b64_e32 v[124:125], v[12:13]
	v_mov_b64_e32 v[122:123], v[10:11]
	v_mov_b64_e32 v[120:121], v[8:9]
	v_mov_b64_e32 v[118:119], v[6:7]
	v_mov_b64_e32 v[116:117], v[4:5]
	v_mov_b64_e32 v[114:115], v[2:3]
	v_mov_b64_e32 v[112:113], v[0:1]
	v_mov_b64_e32 v[108:109], v[12:13]
	v_mov_b64_e32 v[106:107], v[10:11]
	v_mov_b64_e32 v[104:105], v[8:9]
	v_mov_b64_e32 v[102:103], v[6:7]
	v_mov_b64_e32 v[100:101], v[4:5]
	v_mov_b64_e32 v[98:99], v[2:3]
	v_mov_b64_e32 v[96:97], v[0:1]
	v_mov_b64_e32 v[76:77], v[12:13]
	v_mov_b64_e32 v[74:75], v[10:11]
	v_mov_b64_e32 v[72:73], v[8:9]
	v_mov_b64_e32 v[70:71], v[6:7]
	v_mov_b64_e32 v[68:69], v[4:5]
	v_mov_b64_e32 v[66:67], v[2:3]
	v_mov_b64_e32 v[64:65], v[0:1]
	v_mov_b64_e32 v[60:61], v[12:13]
	v_mov_b64_e32 v[58:59], v[10:11]
	v_mov_b64_e32 v[56:57], v[8:9]
	v_mov_b64_e32 v[54:55], v[6:7]
	v_mov_b64_e32 v[52:53], v[4:5]
	v_mov_b64_e32 v[50:51], v[2:3]
	v_mov_b64_e32 v[48:49], v[0:1]
	v_mov_b64_e32 v[28:29], v[12:13]
	v_mov_b64_e32 v[26:27], v[10:11]
	v_mov_b64_e32 v[24:25], v[8:9]
	v_mov_b64_e32 v[22:23], v[6:7]
	v_mov_b64_e32 v[20:21], v[4:5]
	v_mov_b64_e32 v[18:19], v[2:3]
	v_mov_b64_e32 v[16:17], v[0:1]
	v_mov_b64_e32 v[44:45], v[12:13]
	v_mov_b64_e32 v[42:43], v[10:11]
	v_mov_b64_e32 v[40:41], v[8:9]
	v_mov_b64_e32 v[38:39], v[6:7]
	v_mov_b64_e32 v[36:37], v[4:5]
	v_mov_b64_e32 v[34:35], v[2:3]
	v_mov_b64_e32 v[32:33], v[0:1]
	v_mov_b64_e32 v[92:93], v[12:13]
	v_mov_b64_e32 v[90:91], v[10:11]
	v_mov_b64_e32 v[88:89], v[8:9]
	v_mov_b64_e32 v[86:87], v[6:7]
	v_mov_b64_e32 v[84:85], v[4:5]
	v_mov_b64_e32 v[82:83], v[2:3]
	v_mov_b64_e32 v[80:81], v[0:1]
	v_mov_b64_e32 v[140:141], v[12:13]
	v_mov_b64_e32 v[138:139], v[10:11]
	v_mov_b64_e32 v[136:137], v[8:9]
	v_mov_b64_e32 v[134:135], v[6:7]
	v_mov_b64_e32 v[132:133], v[4:5]
	v_mov_b64_e32 v[130:131], v[2:3]
	v_mov_b64_e32 v[128:129], v[0:1]
	s_mov_b32 s49, 0
	s_mov_b32 s86, 0
	s_setprio 1
	s_cmpk_eq_i32 s71, 0x3f00
	s_mov_b64 s[42:43], -1
	s_cbranch_scc0 .LBB0_191

.LBB0_202:
	s_setprio 0
	s_waitcnt lgkmcnt(0)
	v_readlane_b32 s40, v255, 13
	s_nop 1
	v_add_u32_e32 v0, s40, v242
	ds_read_b64_tr_b16 v[160:161], v0 offset:0
	ds_read_b64_tr_b16 v[162:163], v0 offset:0x800
	ds_read_b64_tr_b16 v[164:165], v0 offset:0x200
	ds_read_b64_tr_b16 v[166:167], v0 offset:0xa00
	ds_read_b64_tr_b16 v[168:169], v0 offset:0x400
	ds_read_b64_tr_b16 v[170:171], v0 offset:0xc00
	ds_read_b64_tr_b16 v[172:173], v0 offset:0x600
	ds_read_b64_tr_b16 v[174:175], v0 offset:0xe00
	s_waitcnt lgkmcnt(4)
	s_nop 0
	v_mfma_f32_32x32x16_bf16 v[112:127], v[208:211], v[160:163], v[112:127]
	v_mfma_f32_32x32x16_bf16 v[96:111], v[208:211], v[164:167], v[96:111]
	v_mfma_f32_32x32x16_bf16 v[128:143], v[156:159], v[160:163], v[128:143]
	v_mfma_f32_32x32x16_bf16 v[80:95], v[156:159], v[164:167], v[80:95]
	ds_read_b64_tr_b16 v[160:161], v0 offset:0x1000
	ds_read_b64_tr_b16 v[162:163], v0 offset:0x1800
	ds_read_b64_tr_b16 v[164:165], v0 offset:0x1200
	ds_read_b64_tr_b16 v[166:167], v0 offset:0x1a00
	s_waitcnt lgkmcnt(4)
	v_mfma_f32_32x32x16_bf16 v[64:79], v[208:211], v[168:171], v[64:79]
	v_mfma_f32_32x32x16_bf16 v[48:63], v[208:211], v[172:175], v[48:63]
	v_mfma_f32_32x32x16_bf16 v[32:47], v[156:159], v[168:171], v[32:47]
	v_mfma_f32_32x32x16_bf16 v[16:31], v[156:159], v[172:175], v[16:31]
	ds_read_b64_tr_b16 v[156:157], v0 offset:0x1400
	ds_read_b64_tr_b16 v[158:159], v0 offset:0x1c00
	ds_read_b64_tr_b16 v[168:169], v0 offset:0x1600
	ds_read_b64_tr_b16 v[170:171], v0 offset:0x1e00
	s_waitcnt lgkmcnt(4)
	v_mfma_f32_32x32x16_bf16 v[112:127], v[10:13], v[160:163], v[112:127]
	v_mfma_f32_32x32x16_bf16 v[96:111], v[10:13], v[164:167], v[96:111]
	v_mfma_f32_32x32x16_bf16 v[128:143], v[152:155], v[160:163], v[128:143]
	v_mfma_f32_32x32x16_bf16 v[80:95], v[152:155], v[164:167], v[80:95]
	ds_read_b64_tr_b16 v[160:161], v0 offset:0x2000
	ds_read_b64_tr_b16 v[162:163], v0 offset:0x2800
	ds_read_b64_tr_b16 v[164:165], v0 offset:0x2200
	ds_read_b64_tr_b16 v[166:167], v0 offset:0x2a00
	s_waitcnt lgkmcnt(4)
	v_mfma_f32_32x32x16_bf16 v[64:79], v[10:13], v[156:159], v[64:79]
	v_mfma_f32_32x32x16_bf16 v[48:63], v[10:13], v[168:171], v[48:63]
	v_mfma_f32_32x32x16_bf16 v[32:47], v[152:155], v[156:159], v[32:47]
	v_mfma_f32_32x32x16_bf16 v[16:31], v[152:155], v[168:171], v[16:31]
	ds_read_b64_tr_b16 v[10:11], v0 offset:0x2400
	ds_read_b64_tr_b16 v[12:13], v0 offset:0x2c00
	ds_read_b64_tr_b16 v[152:153], v0 offset:0x2600
	ds_read_b64_tr_b16 v[154:155], v0 offset:0x2e00
	s_waitcnt lgkmcnt(4)
	v_mfma_f32_32x32x16_bf16 v[112:127], v[6:9], v[160:163], v[112:127]
	v_mfma_f32_32x32x16_bf16 v[96:111], v[6:9], v[164:167], v[96:111]
	v_mfma_f32_32x32x16_bf16 v[128:143], v[148:151], v[160:163], v[128:143]
	v_mfma_f32_32x32x16_bf16 v[80:95], v[148:151], v[164:167], v[80:95]
	ds_read_b64_tr_b16 v[156:157], v0 offset:0x3000
	ds_read_b64_tr_b16 v[158:159], v0 offset:0x3800
	ds_read_b64_tr_b16 v[160:161], v0 offset:0x3200
	ds_read_b64_tr_b16 v[162:163], v0 offset:0x3a00
	s_waitcnt lgkmcnt(4)
	v_mfma_f32_32x32x16_bf16 v[64:79], v[6:9], v[10:13], v[64:79]
	v_mfma_f32_32x32x16_bf16 v[48:63], v[6:9], v[152:155], v[48:63]
	v_mfma_f32_32x32x16_bf16 v[32:47], v[148:151], v[10:13], v[32:47]
	v_mfma_f32_32x32x16_bf16 v[16:31], v[148:151], v[152:155], v[16:31]
	ds_read_b64_tr_b16 v[6:7], v0 offset:0x3400
	ds_read_b64_tr_b16 v[8:9], v0 offset:0x3c00
	ds_read_b64_tr_b16 v[10:11], v0 offset:0x3600
	ds_read_b64_tr_b16 v[12:13], v0 offset:0x3e00
	s_waitcnt lgkmcnt(4)
	v_mfma_f32_32x32x16_bf16 v[112:127], v[2:5], v[156:159], v[112:127]
	v_mfma_f32_32x32x16_bf16 v[96:111], v[2:5], v[160:163], v[96:111]
	v_mfma_f32_32x32x16_bf16 v[128:143], v[144:147], v[156:159], v[128:143]
	v_mfma_f32_32x32x16_bf16 v[80:95], v[144:147], v[160:163], v[80:95]
	s_waitcnt lgkmcnt(0)
	v_mfma_f32_32x32x16_bf16 v[64:79], v[2:5], v[6:9], v[64:79]
	v_mfma_f32_32x32x16_bf16 v[48:63], v[2:5], v[10:13], v[48:63]
	v_mfma_f32_32x32x16_bf16 v[32:47], v[144:147], v[6:9], v[32:47]
	v_mfma_f32_32x32x16_bf16 v[16:31], v[144:147], v[10:13], v[16:31]
	s_mov_b64 s[40:41], 0
